# speedup vs baseline: 1.0109x; 1.0000x over previous
.LBB2_7:
	v_and_b32_e32 v216, 1, v0
	v_bfe_u32 v217, v0, 1, 1
	v_cmp_ne_u32_e64 s[90:91], 0, v216
	v_cmp_ne_u32_e64 s[92:93], 0, v217
	v_mul_u32_u24_e32 v224, 60, v216
	v_mul_u32_u24_e32 v218, 0x1f8, v217
	v_add_u32_e32 v224, v224, v218
	v_fmamk_f32 v126, v126, 0x3a800000, v158
	v_fmamk_f32 v127, v127, 0x3a800000, v159
	v_mov_b32_e32 v178, v163
	v_cvt_pk_fp8_f32 v178, v126, v127
	v_fmamk_f32 v126, v128, 0x3a800000, v160
	v_fmamk_f32 v122, v122, 0x3a800000, v158
	v_fmamk_f32 v123, v123, 0x3a800000, v159
	v_mov_b32_e32 v128, v163
	v_cvt_pk_fp8_f32 v128, v122, v123
	v_fmamk_f32 v124, v124, 0x3a800000, v160
	v_fmamk_f32 v125, v125, 0x3a800000, v161
	v_fmamk_f32 v118, v118, 0x3a800000, v158
	v_cvt_pk_fp8_f32 v128, v124, v125 op_sel:[0,0,1]
	v_fmamk_f32 v119, v119, 0x3a800000, v159
	v_mov_b32_e32 v124, v163
	v_cvt_pk_fp8_f32 v124, v118, v119
	v_fmamk_f32 v114, v114, 0x3a800000, v158
	v_fmamk_f32 v115, v115, 0x3a800000, v159
	v_mov_b32_e32 v118, v163
	v_cvt_pk_fp8_f32 v118, v114, v115
	v_fmamk_f32 v114, v116, 0x3a800000, v160
	v_fmamk_f32 v110, v110, 0x3a800000, v154
	v_fmamk_f32 v111, v111, 0x3a800000, v155
	v_mov_b32_e32 v116, v163
	v_cvt_pk_fp8_f32 v116, v110, v111
	v_fmamk_f32 v112, v112, 0x3a800000, v156
	v_fmamk_f32 v113, v113, 0x3a800000, v157
	v_fmamk_f32 v98, v98, 0x3a800000, v154
	v_cvt_pk_fp8_f32 v116, v112, v113 op_sel:[0,0,1]
	v_fmamk_f32 v99, v99, 0x3a800000, v155
	v_mov_b32_e32 v112, v163
	v_cvt_pk_fp8_f32 v112, v98, v99
	v_fmamk_f32 v100, v100, 0x3a800000, v156
	v_fmamk_f32 v101, v101, 0x3a800000, v157
	v_and_b32_e32 v162, 15, v175
	v_cvt_pk_fp8_f32 v112, v100, v101 op_sel:[0,0,1]
	v_fmamk_f32 v100, v106, 0x3a800000, v154
	v_fmamk_f32 v101, v107, 0x3a800000, v155
	v_fmamk_f32 v106, v108, 0x3a800000, v156
	v_mov_b32_e32 v108, v163
	v_cvt_pk_fp8_f32 v108, v100, v101
	v_fmamk_f32 v100, v102, 0x3a800000, v154
	v_fmamk_f32 v101, v103, 0x3a800000, v155
	v_mov_b32_e32 v102, v163
	v_cvt_pk_fp8_f32 v102, v100, v101
	v_lshrrev_b32_e32 v175, 1, v175
	v_and_b32_e32 v175, 0x60, v175
	v_or3_b32 v162, v175, v162, s50
	v_lshrrev_b32_e32 v175, 2, v173
	v_fmamk_f32 v107, v109, 0x3a800000, v157
	v_fmamk_f32 v100, v104, 0x3a800000, v156
	v_fmac_f32_e32 v157, 0x3a800000, v105
	v_and_b32_e32 v175, 0xf0, v175
	v_cvt_pk_fp8_f32 v102, v100, v157 op_sel:[0,0,1]
	v_fmamk_f32 v86, v86, 0x3a800000, v150
	v_fmamk_f32 v87, v87, 0x3a800000, v151
	v_mov_b32_e32 v100, v163
	s_ashr_i32 s45, s50, 4
	v_or_b32_e32 v175, s56, v175
	v_fmamk_f32 v127, v129, 0x3a800000, v161
	v_fmamk_f32 v121, v121, 0x3a800000, v161
	v_fmac_f32_e32 v161, 0x3a800000, v117
	v_cvt_pk_fp8_f32 v100, v86, v87
	s_and_b32 s45, s45, 0xffffff00
	v_cvt_pk_fp8_f32 v118, v114, v161 op_sel:[0,0,1]
	v_or_b32_e32 v114, 4, v175
	v_add_u32_e32 v176, s45, v175
	v_add_u32_e32 v114, s45, v114
	v_or_b32_e32 v176, v176, v172
	v_or_b32_e32 v114, v114, v172
	v_fmamk_f32 v88, v88, 0x3a800000, v152
	v_fmamk_f32 v89, v89, 0x3a800000, v153
	v_ashrrev_i32_e32 v177, 31, v176
	v_cvt_pk_fp8_f32 v178, v126, v127 op_sel:[0,0,1]
	v_ashrrev_i32_e32 v115, 31, v114
	v_cvt_pk_fp8_f32 v100, v88, v89 op_sel:[0,0,1]
	v_fmamk_f32 v82, v82, 0x3a800000, v150
	v_fmamk_f32 v83, v83, 0x3a800000, v151
	v_mov_b32_e32 v88, v163
	v_lshlrev_b64 v[176:177], 14, v[176:177]
	v_lshlrev_b32_e32 v162, 2, v162
	v_fmamk_f32 v120, v120, 0x3a800000, v160
	v_lshlrev_b64 v[110:111], 14, v[114:115]
	v_cvt_pk_fp8_f32 v88, v82, v83
	v_and_b32_e32 v162, 0x3dbc, v162
	v_add_u32_e32 v162, v162, v224
	v_lshl_add_u64 v[126:127], s[18:19], 0, v[176:177]
	v_cvt_pk_fp8_f32 v124, v120, v121 op_sel:[0,0,1]
	v_lshl_add_u64 v[110:111], s[18:19], 0, v[110:111]
	v_cvt_pk_fp8_f32 v108, v106, v107 op_sel:[0,0,1]
	v_lshl_add_u64 v[122:123], v[126:127], 0, v[162:163]
	v_lshl_add_u64 v[98:99], v[110:111], 0, v[162:163]
	s_nop 0
	v_cndmask_b32_e64 v216, v124, v178, s[92:93]
	v_cndmask_b32_e64 v217, v118, v128, s[92:93]
	s_nop 0
	v_mov_b32_dpp v218, v216 quad_perm:[2,3,0,1] row_mask:0xf bank_mask:0xf
	v_mov_b32_dpp v219, v217 quad_perm:[2,3,0,1] row_mask:0xf bank_mask:0xf
	v_cndmask_b32_e64 v220, v178, v218, s[92:93]
	v_cndmask_b32_e64 v221, v128, v219, s[92:93]
	v_cndmask_b32_e64 v222, v218, v124, s[92:93]
	v_cndmask_b32_e64 v223, v219, v118, s[92:93]
	v_cndmask_b32_e64 v216, v221, v220, s[90:91]
	v_cndmask_b32_e64 v217, v223, v222, s[90:91]
	s_nop 0
	v_mov_b32_dpp v218, v216 quad_perm:[1,0,3,2] row_mask:0xf bank_mask:0xf
	v_mov_b32_dpp v219, v217 quad_perm:[1,0,3,2] row_mask:0xf bank_mask:0xf
	v_cndmask_b32_e64 v184, v220, v218, s[90:91]
	v_cndmask_b32_e64 v185, v218, v221, s[90:91]
	v_cndmask_b32_e64 v186, v222, v219, s[90:91]
	v_cndmask_b32_e64 v187, v219, v223, s[90:91]
	global_store_dwordx4 v[122:123], v[184:187], off sc1
	s_nop 0
	v_cndmask_b32_e64 v216, v108, v116, s[92:93]
	v_cndmask_b32_e64 v217, v102, v112, s[92:93]
	s_nop 0
	v_mov_b32_dpp v218, v216 quad_perm:[2,3,0,1] row_mask:0xf bank_mask:0xf
	v_mov_b32_dpp v219, v217 quad_perm:[2,3,0,1] row_mask:0xf bank_mask:0xf
	v_cndmask_b32_e64 v220, v116, v218, s[92:93]
	v_cndmask_b32_e64 v221, v112, v219, s[92:93]
	v_cndmask_b32_e64 v222, v218, v108, s[92:93]
	v_cndmask_b32_e64 v223, v219, v102, s[92:93]
	v_cndmask_b32_e64 v216, v221, v220, s[90:91]
	v_cndmask_b32_e64 v217, v223, v222, s[90:91]
	s_nop 0
	v_mov_b32_dpp v218, v216 quad_perm:[1,0,3,2] row_mask:0xf bank_mask:0xf
	v_mov_b32_dpp v219, v217 quad_perm:[1,0,3,2] row_mask:0xf bank_mask:0xf
	v_cndmask_b32_e64 v188, v220, v218, s[90:91]
	v_cndmask_b32_e64 v189, v218, v221, s[90:91]
	v_cndmask_b32_e64 v190, v222, v219, s[90:91]
	v_cndmask_b32_e64 v191, v219, v223, s[90:91]
	global_store_dwordx4 v[98:99], v[188:191], off sc1
	v_or_b32_e32 v98, 8, v175
	v_fmamk_f32 v84, v84, 0x3a800000, v152
	v_fmamk_f32 v85, v85, 0x3a800000, v153
	v_add_u32_e32 v98, s45, v98
	v_cvt_pk_fp8_f32 v88, v84, v85 op_sel:[0,0,1]
	v_fmamk_f32 v84, v94, 0x3a800000, v150
	v_fmamk_f32 v85, v95, 0x3a800000, v151
	v_mov_b32_e32 v89, v163
	v_or_b32_e32 v98, v98, v172
	v_cvt_pk_fp8_f32 v89, v84, v85
	v_fmamk_f32 v84, v90, 0x3a800000, v150
	v_fmamk_f32 v85, v91, 0x3a800000, v151
	v_mov_b32_e32 v90, v163
	v_ashrrev_i32_e32 v99, 31, v98
	v_cvt_pk_fp8_f32 v90, v84, v85
	v_lshlrev_b64 v[86:87], 14, v[98:99]
	v_lshl_add_u64 v[86:87], s[18:19], 0, v[86:87]
	v_lshl_add_u64 v[82:83], v[86:87], 0, v[162:163]
	v_fmamk_f32 v87, v97, 0x3a800000, v153
	v_fmamk_f32 v84, v92, 0x3a800000, v152
	v_fmac_f32_e32 v153, 0x3a800000, v93
	v_cvt_pk_fp8_f32 v90, v84, v153 op_sel:[0,0,1]
	v_fmamk_f32 v66, v66, 0x3a800000, v146
	v_fmamk_f32 v67, v67, 0x3a800000, v147
	v_mov_b32_e32 v84, v163
	v_cvt_pk_fp8_f32 v84, v66, v67
	v_fmamk_f32 v68, v68, 0x3a800000, v148
	v_fmamk_f32 v69, v69, 0x3a800000, v149
	v_fmamk_f32 v50, v50, 0x3a800000, v146
	v_cvt_pk_fp8_f32 v84, v68, v69 op_sel:[0,0,1]
	v_fmamk_f32 v51, v51, 0x3a800000, v147
	v_mov_b32_e32 v68, v163
	v_fmamk_f32 v86, v96, 0x3a800000, v152
	v_cvt_pk_fp8_f32 v68, v50, v51
	v_cvt_pk_fp8_f32 v89, v86, v87 op_sel:[0,0,1]
	s_nop 0
	v_cndmask_b32_e64 v216, v89, v100, s[92:93]
	v_cndmask_b32_e64 v217, v90, v88, s[92:93]
	s_nop 0
	v_mov_b32_dpp v218, v216 quad_perm:[2,3,0,1] row_mask:0xf bank_mask:0xf
	v_mov_b32_dpp v219, v217 quad_perm:[2,3,0,1] row_mask:0xf bank_mask:0xf
	v_cndmask_b32_e64 v220, v100, v218, s[92:93]
	v_cndmask_b32_e64 v221, v88, v219, s[92:93]
	v_cndmask_b32_e64 v222, v218, v89, s[92:93]
	v_cndmask_b32_e64 v223, v219, v90, s[92:93]
	v_cndmask_b32_e64 v216, v221, v220, s[90:91]
	v_cndmask_b32_e64 v217, v223, v222, s[90:91]
	s_nop 0
	v_mov_b32_dpp v218, v216 quad_perm:[1,0,3,2] row_mask:0xf bank_mask:0xf
	v_mov_b32_dpp v219, v217 quad_perm:[1,0,3,2] row_mask:0xf bank_mask:0xf
	v_cndmask_b32_e64 v192, v220, v218, s[90:91]
	v_cndmask_b32_e64 v193, v218, v221, s[90:91]
	v_cndmask_b32_e64 v194, v222, v219, s[90:91]
	v_cndmask_b32_e64 v195, v219, v223, s[90:91]
	global_store_dwordx4 v[82:83], v[192:195], off sc1
	v_or_b32_e32 v82, 12, v175
	v_fmamk_f32 v52, v52, 0x3a800000, v148
	v_fmamk_f32 v53, v53, 0x3a800000, v149
	v_add_u32_e32 v82, s45, v82
	v_cvt_pk_fp8_f32 v68, v52, v53 op_sel:[0,0,1]
	v_fmamk_f32 v52, v78, 0x3a800000, v146
	v_fmamk_f32 v53, v79, 0x3a800000, v147
	v_mov_b32_e32 v69, v163
	v_or_b32_e32 v82, v82, v172
	v_cvt_pk_fp8_f32 v69, v52, v53
	v_fmamk_f32 v52, v74, 0x3a800000, v146
	v_fmamk_f32 v53, v75, 0x3a800000, v147
	v_mov_b32_e32 v74, v163
	v_ashrrev_i32_e32 v83, 31, v82
	v_cvt_pk_fp8_f32 v74, v52, v53
	v_lshlrev_b64 v[66:67], 14, v[82:83]
	v_lshl_add_u64 v[66:67], s[18:19], 0, v[66:67]
	v_lshl_add_u64 v[50:51], v[66:67], 0, v[162:163]
	v_fmamk_f32 v67, v81, 0x3a800000, v149
	v_fmamk_f32 v52, v76, 0x3a800000, v148
	v_fmac_f32_e32 v149, 0x3a800000, v77
	v_cvt_pk_fp8_f32 v74, v52, v149 op_sel:[0,0,1]
	v_fmamk_f32 v52, v62, 0x3a800000, v142
	v_fmamk_f32 v53, v63, 0x3a800000, v143
	v_mov_b32_e32 v62, v163
	v_cvt_pk_fp8_f32 v62, v52, v53
	v_fmamk_f32 v52, v64, 0x3a800000, v144
	v_fmamk_f32 v53, v65, 0x3a800000, v145
	v_fmamk_f32 v66, v80, 0x3a800000, v148
	v_cvt_pk_fp8_f32 v62, v52, v53 op_sel:[0,0,1]
	v_fmamk_f32 v52, v54, 0x3a800000, v142
	v_fmamk_f32 v53, v55, 0x3a800000, v143
	v_mov_b32_e32 v54, v163
	v_cvt_pk_fp8_f32 v54, v52, v53
	v_fmamk_f32 v52, v56, 0x3a800000, v144
	v_fmamk_f32 v53, v57, 0x3a800000, v145
	v_mov_b32_e32 v57, v163
	v_cvt_pk_fp8_f32 v54, v52, v53 op_sel:[0,0,1]
	v_fmamk_f32 v52, v70, 0x3a800000, v142
	v_fmamk_f32 v53, v71, 0x3a800000, v143
	v_cvt_pk_fp8_f32 v69, v66, v67 op_sel:[0,0,1]
	v_cvt_pk_fp8_f32 v57, v52, v53
	v_fmamk_f32 v52, v58, 0x3a800000, v142
	v_fmamk_f32 v53, v59, 0x3a800000, v143
	v_mov_b32_e32 v58, v163
	v_cvt_pk_fp8_f32 v58, v52, v53
	s_nop 0
	v_cndmask_b32_e64 v216, v69, v84, s[92:93]
	v_cndmask_b32_e64 v217, v74, v68, s[92:93]
	s_nop 0
	v_mov_b32_dpp v218, v216 quad_perm:[2,3,0,1] row_mask:0xf bank_mask:0xf
	v_mov_b32_dpp v219, v217 quad_perm:[2,3,0,1] row_mask:0xf bank_mask:0xf
	v_cndmask_b32_e64 v220, v84, v218, s[92:93]
	v_cndmask_b32_e64 v221, v68, v219, s[92:93]
	v_cndmask_b32_e64 v222, v218, v69, s[92:93]
	v_cndmask_b32_e64 v223, v219, v74, s[92:93]
	v_cndmask_b32_e64 v216, v221, v220, s[90:91]
	v_cndmask_b32_e64 v217, v223, v222, s[90:91]
	s_nop 0
	v_mov_b32_dpp v218, v216 quad_perm:[1,0,3,2] row_mask:0xf bank_mask:0xf
	v_mov_b32_dpp v219, v217 quad_perm:[1,0,3,2] row_mask:0xf bank_mask:0xf
	v_cndmask_b32_e64 v196, v220, v218, s[90:91]
	v_cndmask_b32_e64 v197, v218, v221, s[90:91]
	v_cndmask_b32_e64 v198, v222, v219, s[90:91]
	v_cndmask_b32_e64 v199, v219, v223, s[90:91]
	global_store_dwordx4 v[50:51], v[196:199], off sc1
	v_lshrrev_b32_e32 v50, 2, v174
	v_and_b32_e32 v50, 0xf0, v50
	v_or_b32_e32 v50, s56, v50
	v_fmamk_f32 v56, v73, 0x3a800000, v145
	v_fmamk_f32 v52, v60, 0x3a800000, v144
	v_fmac_f32_e32 v145, 0x3a800000, v61
	v_add_u32_e32 v50, s45, v50
	v_cvt_pk_fp8_f32 v58, v52, v145 op_sel:[0,0,1]
	v_fmamk_f32 v42, v42, 0x3a800000, v138
	v_fmamk_f32 v43, v43, 0x3a800000, v139
	v_mov_b32_e32 v52, v163
	v_or_b32_e32 v50, v50, v172
	v_cvt_pk_fp8_f32 v52, v42, v43
	v_ashrrev_i32_e32 v51, 31, v50
	v_lshlrev_b64 v[50:51], 14, v[50:51]
	v_fmamk_f32 v55, v72, 0x3a800000, v144
	v_lshl_add_u64 v[50:51], s[18:19], 0, v[50:51]
	v_cvt_pk_fp8_f32 v57, v55, v56 op_sel:[0,0,1]
	v_fmamk_f32 v44, v44, 0x3a800000, v140
	v_fmamk_f32 v45, v45, 0x3a800000, v141
	v_lshl_add_u64 v[50:51], v[50:51], 0, v[162:163]
	v_cvt_pk_fp8_f32 v52, v44, v45 op_sel:[0,0,1]
	v_fmamk_f32 v34, v34, 0x3a800000, v138
	v_fmamk_f32 v35, v35, 0x3a800000, v139
	v_mov_b32_e32 v44, v163
	s_nop 0
	v_cndmask_b32_e64 v216, v57, v62, s[92:93]
	v_cndmask_b32_e64 v217, v58, v54, s[92:93]
	s_nop 0
	v_mov_b32_dpp v218, v216 quad_perm:[2,3,0,1] row_mask:0xf bank_mask:0xf
	v_mov_b32_dpp v219, v217 quad_perm:[2,3,0,1] row_mask:0xf bank_mask:0xf
	v_cndmask_b32_e64 v220, v62, v218, s[92:93]
	v_cndmask_b32_e64 v221, v54, v219, s[92:93]
	v_cndmask_b32_e64 v222, v218, v57, s[92:93]
	v_cndmask_b32_e64 v223, v219, v58, s[92:93]
	v_cndmask_b32_e64 v216, v221, v220, s[90:91]
	v_cndmask_b32_e64 v217, v223, v222, s[90:91]
	s_nop 0
	v_mov_b32_dpp v218, v216 quad_perm:[1,0,3,2] row_mask:0xf bank_mask:0xf
	v_mov_b32_dpp v219, v217 quad_perm:[1,0,3,2] row_mask:0xf bank_mask:0xf
	v_cndmask_b32_e64 v200, v220, v218, s[90:91]
	v_cndmask_b32_e64 v201, v218, v221, s[90:91]
	v_cndmask_b32_e64 v202, v222, v219, s[90:91]
	v_cndmask_b32_e64 v203, v219, v223, s[90:91]
	global_store_dwordx4 v[50:51], v[200:203], off sc1
	v_add_u32_e32 v50, 0x90, v173
	v_cvt_pk_fp8_f32 v44, v34, v35
	v_lshrrev_b32_e32 v50, 2, v50
	v_and_b32_e32 v50, 0xf4, v50
	v_or_b32_e32 v50, s56, v50
	v_fmamk_f32 v36, v36, 0x3a800000, v140
	v_fmamk_f32 v37, v37, 0x3a800000, v141
	v_add_u32_e32 v50, s45, v50
	v_cvt_pk_fp8_f32 v44, v36, v37 op_sel:[0,0,1]
	v_fmamk_f32 v36, v46, 0x3a800000, v138
	v_fmamk_f32 v37, v47, 0x3a800000, v139
	v_mov_b32_e32 v45, v163
	v_or_b32_e32 v50, v50, v172
	v_cvt_pk_fp8_f32 v45, v36, v37
	v_fmamk_f32 v36, v38, 0x3a800000, v138
	v_fmamk_f32 v37, v39, 0x3a800000, v139
	v_mov_b32_e32 v38, v163
	v_ashrrev_i32_e32 v51, 31, v50
	v_cvt_pk_fp8_f32 v38, v36, v37
	v_lshlrev_b64 v[42:43], 14, v[50:51]
	v_lshl_add_u64 v[42:43], s[18:19], 0, v[42:43]
	v_lshl_add_u64 v[34:35], v[42:43], 0, v[162:163]
	v_fmamk_f32 v43, v49, 0x3a800000, v141
	v_fmamk_f32 v36, v40, 0x3a800000, v140
	v_fmac_f32_e32 v141, 0x3a800000, v41
	v_cvt_pk_fp8_f32 v38, v36, v141 op_sel:[0,0,1]
	v_fmamk_f32 v26, v26, 0x3a800000, v134
	v_fmamk_f32 v27, v27, 0x3a800000, v135
	v_mov_b32_e32 v36, v163
	v_cvt_pk_fp8_f32 v36, v26, v27
	v_fmamk_f32 v42, v48, 0x3a800000, v140
	v_cvt_pk_fp8_f32 v45, v42, v43 op_sel:[0,0,1]
	v_fmamk_f32 v28, v28, 0x3a800000, v136
	v_fmamk_f32 v29, v29, 0x3a800000, v137
	v_cvt_pk_fp8_f32 v36, v28, v29 op_sel:[0,0,1]
	v_fmamk_f32 v18, v18, 0x3a800000, v134
	v_fmamk_f32 v19, v19, 0x3a800000, v135
	v_mov_b32_e32 v28, v163
	s_nop 0
	v_cndmask_b32_e64 v216, v45, v52, s[92:93]
	v_cndmask_b32_e64 v217, v38, v44, s[92:93]
	s_nop 0
	v_mov_b32_dpp v218, v216 quad_perm:[2,3,0,1] row_mask:0xf bank_mask:0xf
	v_mov_b32_dpp v219, v217 quad_perm:[2,3,0,1] row_mask:0xf bank_mask:0xf
	v_cndmask_b32_e64 v220, v52, v218, s[92:93]
	v_cndmask_b32_e64 v221, v44, v219, s[92:93]
	v_cndmask_b32_e64 v222, v218, v45, s[92:93]
	v_cndmask_b32_e64 v223, v219, v38, s[92:93]
	v_cndmask_b32_e64 v216, v221, v220, s[90:91]
	v_cndmask_b32_e64 v217, v223, v222, s[90:91]
	s_nop 0
	v_mov_b32_dpp v218, v216 quad_perm:[1,0,3,2] row_mask:0xf bank_mask:0xf
	v_mov_b32_dpp v219, v217 quad_perm:[1,0,3,2] row_mask:0xf bank_mask:0xf
	v_cndmask_b32_e64 v204, v220, v218, s[90:91]
	v_cndmask_b32_e64 v205, v218, v221, s[90:91]
	v_cndmask_b32_e64 v206, v222, v219, s[90:91]
	v_cndmask_b32_e64 v207, v219, v223, s[90:91]
	global_store_dwordx4 v[34:35], v[204:207], off sc1
	v_add_u32_e32 v34, 0xa0, v173
	v_cvt_pk_fp8_f32 v28, v18, v19
	v_lshrrev_b32_e32 v34, 2, v34
	v_and_b32_e32 v34, 0xf8, v34
	v_or_b32_e32 v34, s56, v34
	v_fmamk_f32 v20, v20, 0x3a800000, v136
	v_fmamk_f32 v21, v21, 0x3a800000, v137
	v_add_u32_e32 v34, s45, v34
	v_cvt_pk_fp8_f32 v28, v20, v21 op_sel:[0,0,1]
	v_fmamk_f32 v20, v30, 0x3a800000, v134
	v_fmamk_f32 v21, v31, 0x3a800000, v135
	v_mov_b32_e32 v29, v163
	v_or_b32_e32 v34, v34, v172
	v_cvt_pk_fp8_f32 v29, v20, v21
	v_fmamk_f32 v20, v22, 0x3a800000, v134
	v_fmamk_f32 v21, v23, 0x3a800000, v135
	v_mov_b32_e32 v22, v163
	v_ashrrev_i32_e32 v35, 31, v34
	v_cvt_pk_fp8_f32 v22, v20, v21
	v_lshlrev_b64 v[26:27], 14, v[34:35]
	v_lshl_add_u64 v[26:27], s[18:19], 0, v[26:27]
	v_lshl_add_u64 v[18:19], v[26:27], 0, v[162:163]
	v_fmamk_f32 v27, v33, 0x3a800000, v137
	v_fmamk_f32 v20, v24, 0x3a800000, v136
	v_fmac_f32_e32 v137, 0x3a800000, v25
	v_cvt_pk_fp8_f32 v22, v20, v137 op_sel:[0,0,1]
	v_fmamk_f32 v10, v10, 0x3a800000, v130
	v_fmamk_f32 v11, v11, 0x3a800000, v131
	v_mov_b32_e32 v20, v163
	v_cvt_pk_fp8_f32 v20, v10, v11
	v_fmamk_f32 v26, v32, 0x3a800000, v136
	v_cvt_pk_fp8_f32 v29, v26, v27 op_sel:[0,0,1]
	v_fmamk_f32 v12, v12, 0x3a800000, v132
	v_fmamk_f32 v13, v13, 0x3a800000, v133
	s_nop 0
	v_cndmask_b32_e64 v216, v29, v36, s[92:93]
	v_cndmask_b32_e64 v217, v22, v28, s[92:93]
	s_nop 0
	v_mov_b32_dpp v218, v216 quad_perm:[2,3,0,1] row_mask:0xf bank_mask:0xf
	v_mov_b32_dpp v219, v217 quad_perm:[2,3,0,1] row_mask:0xf bank_mask:0xf
	v_cndmask_b32_e64 v220, v36, v218, s[92:93]
	v_cndmask_b32_e64 v221, v28, v219, s[92:93]
	v_cndmask_b32_e64 v222, v218, v29, s[92:93]
	v_cndmask_b32_e64 v223, v219, v22, s[92:93]
	v_cndmask_b32_e64 v216, v221, v220, s[90:91]
	v_cndmask_b32_e64 v217, v223, v222, s[90:91]
	s_nop 0
	v_mov_b32_dpp v218, v216 quad_perm:[1,0,3,2] row_mask:0xf bank_mask:0xf
	v_mov_b32_dpp v219, v217 quad_perm:[1,0,3,2] row_mask:0xf bank_mask:0xf
	v_cndmask_b32_e64 v208, v220, v218, s[90:91]
	v_cndmask_b32_e64 v209, v218, v221, s[90:91]
	v_cndmask_b32_e64 v210, v222, v219, s[90:91]
	v_cndmask_b32_e64 v211, v219, v223, s[90:91]
	global_store_dwordx4 v[18:19], v[208:211], off sc1
	v_add_u32_e32 v18, 0xb0, v173
	v_cvt_pk_fp8_f32 v20, v12, v13 op_sel:[0,0,1]
	v_fmamk_f32 v2, v2, 0x3a800000, v130
	v_fmamk_f32 v3, v3, 0x3a800000, v131
	v_mov_b32_e32 v12, v163
	v_lshrrev_b32_e32 v18, 2, v18
	v_cvt_pk_fp8_f32 v12, v2, v3
	v_and_b32_e32 v18, 0xfc, v18
	v_or_b32_e32 v18, s56, v18
	v_add_u32_e32 v18, s45, v18
	v_fmamk_f32 v4, v4, 0x3a800000, v132
	v_fmamk_f32 v5, v5, 0x3a800000, v133
	v_or_b32_e32 v18, v18, v172
	v_cvt_pk_fp8_f32 v12, v4, v5 op_sel:[0,0,1]
	v_fmamk_f32 v4, v14, 0x3a800000, v130
	v_fmamk_f32 v5, v15, 0x3a800000, v131
	v_mov_b32_e32 v13, v163
	v_ashrrev_i32_e32 v19, 31, v18
	v_cvt_pk_fp8_f32 v13, v4, v5
	v_fmamk_f32 v4, v6, 0x3a800000, v130
	v_fmamk_f32 v5, v7, 0x3a800000, v131
	v_mov_b32_e32 v6, v163
	v_lshlrev_b64 v[10:11], 14, v[18:19]
	v_cvt_pk_fp8_f32 v6, v4, v5
	v_lshl_add_u64 v[10:11], s[18:19], 0, v[10:11]
	v_lshl_add_u64 v[2:3], v[10:11], 0, v[162:163]
	v_fmamk_f32 v10, v16, 0x3a800000, v132
	v_fmamk_f32 v11, v17, 0x3a800000, v133
	v_cvt_pk_fp8_f32 v13, v10, v11 op_sel:[0,0,1]
	v_fmamk_f32 v4, v8, 0x3a800000, v132
	v_fmac_f32_e32 v133, 0x3a800000, v9
	v_cvt_pk_fp8_f32 v6, v4, v133 op_sel:[0,0,1]
	s_mov_b64 s[56:57], 0
	s_andn2_b64 vcc, exec, s[52:53]
	s_mov_b32 s50, s54
	s_nop 0
	v_cndmask_b32_e64 v216, v13, v20, s[92:93]
	v_cndmask_b32_e64 v217, v6, v12, s[92:93]
	s_nop 0
	v_mov_b32_dpp v218, v216 quad_perm:[2,3,0,1] row_mask:0xf bank_mask:0xf
	v_mov_b32_dpp v219, v217 quad_perm:[2,3,0,1] row_mask:0xf bank_mask:0xf
	v_cndmask_b32_e64 v220, v20, v218, s[92:93]
	v_cndmask_b32_e64 v221, v12, v219, s[92:93]
	v_cndmask_b32_e64 v222, v218, v13, s[92:93]
	v_cndmask_b32_e64 v223, v219, v6, s[92:93]
	v_cndmask_b32_e64 v216, v221, v220, s[90:91]
	v_cndmask_b32_e64 v217, v223, v222, s[90:91]
	s_nop 0
	v_mov_b32_dpp v218, v216 quad_perm:[1,0,3,2] row_mask:0xf bank_mask:0xf
	v_mov_b32_dpp v219, v217 quad_perm:[1,0,3,2] row_mask:0xf bank_mask:0xf
	v_cndmask_b32_e64 v212, v220, v218, s[90:91]
	v_cndmask_b32_e64 v213, v218, v221, s[90:91]
	v_cndmask_b32_e64 v214, v222, v219, s[90:91]
	v_cndmask_b32_e64 v215, v219, v223, s[90:91]
	global_store_dwordx4 v[2:3], v[212:215], off sc1
	s_cbranch_vccz .LBB2_26

.LBB2_10:
	s_or_b64 exec, exec, s[52:53]
	s_xor_b64 s[54:55], s[56:57], -1
	s_mov_b64 s[52:53], -1
	s_and_b64 vcc, exec, s[54:55]
	s_cbranch_vccz .LBB2_12
	s_waitcnt vmcnt(8)
	s_mov_b32 s87, 1
	s_mov_b64 s[52:53], 0

.LBB2_14:
	s_ashr_i32 s51, s50, 31
	s_lshl_b64 s[52:53], s[50:51], 10
	s_add_u32 s52, s10, s52
	s_addc_u32 s53, s11, s53
	v_mov_b32_e32 v162, v1
	s_barrier
	s_add_i32 s78, s70, 0x18000
	v_lshl_add_u64 v[2:3], s[52:53], 0, v[162:163]
	s_ashr_i32 s45, s44, 31
	v_lshl_add_u64 v[2:3], v[2:3], 0, s[20:21]
	s_mov_b32 m0, s78
	v_mov_b32_e32 v162, v1
	s_add_i32 s79, s70, 0x1a000
	s_lshl_b64 s[54:55], s[44:45], 10
	global_load_lds_dwordx4 v[2:3], off
	s_add_u32 s54, s8, s54
	v_lshl_add_u64 v[2:3], s[52:53], 0, v[162:163]
	v_lshl_add_u64 v[2:3], v[2:3], 0, s[22:23]
	s_mov_b32 m0, s79
	s_addc_u32 s55, s9, s55
	v_mov_b32_e32 v162, v1
	s_or_b32 s56, s50, 0x80
	global_load_lds_dwordx4 v[2:3], off
	s_add_i32 s45, s70, 0x8000
	v_lshl_add_u64 v[2:3], s[54:55], 0, v[162:163]
	s_ashr_i32 s57, s56, 31
	v_lshl_add_u64 v[2:3], v[2:3], 0, s[20:21]
	s_mov_b32 m0, s45
	v_mov_b32_e32 v162, v1
	s_add_i32 s80, s70, 0xa000
	s_lshl_b64 s[56:57], s[56:57], 10
	global_load_lds_dwordx4 v[2:3], off
	s_add_u32 s56, s10, s56
	v_lshl_add_u64 v[2:3], s[54:55], 0, v[162:163]
	v_lshl_add_u64 v[2:3], v[2:3], 0, s[22:23]
	s_mov_b32 m0, s80
	s_addc_u32 s57, s11, s57
	v_mov_b32_e32 v162, v1
	global_load_lds_dwordx4 v[2:3], off
	s_add_i32 s82, s70, 0x1c000
	v_lshl_add_u64 v[2:3], s[56:57], 0, v[162:163]
	v_lshl_add_u64 v[2:3], v[2:3], 0, s[20:21]
	s_mov_b32 m0, s82
	v_mov_b32_e32 v162, v1
	global_load_lds_dwordx4 v[2:3], off
	s_add_i32 s84, s70, 0x1e000
	v_lshl_add_u64 v[2:3], s[56:57], 0, v[162:163]
	v_lshl_add_u64 v[2:3], v[2:3], 0, s[22:23]
	s_mov_b32 m0, s84
	v_mov_b32_e32 v50, 0
	global_load_lds_dwordx4 v[2:3], off
	s_waitcnt lgkmcnt(0)
	s_lshr_b32 s86, s44, 10
	s_cmp_eq_u32 s86, 1
	s_cselect_b32 s88, s14, s6
	s_cselect_b32 s89, s15, s7
	s_cmp_eq_u32 s86, 0
	s_cselect_b32 s88, s12, s88
	s_cselect_b32 s89, s13, s89
	s_and_b32 s86, s44, 0x3ff
	s_lshl_b32 s86, s86, 2
	s_add_u32 s88, s88, s86
	s_addc_u32 s89, s89, 0
	v_and_b32_e32 v184, 63, v0
	v_lshlrev_b32_e32 v184, 4, v184
	s_mov_b32 m0, 0x20000
	s_nop 0
	global_load_lds_dwordx4 v184, s[88:89]
	s_cmp_eq_u32 s87, 0
	s_cbranch_scc1 .Lg2_w6
	s_waitcnt vmcnt(15)
	s_branch .Lg2_wd

	.amdhsa_kernel _Z6k_gemmILi2EEvPKtS1_PvPKfS4_S4_ii
		.amdhsa_group_segment_fixed_size 1024
		.amdhsa_private_segment_fixed_size 0
		.amdhsa_kernarg_size 56
		.amdhsa_user_sgpr_count 2
		.amdhsa_user_sgpr_dispatch_ptr 0
		.amdhsa_user_sgpr_queue_ptr 0
		.amdhsa_user_sgpr_kernarg_segment_ptr 1
		.amdhsa_user_sgpr_dispatch_id 0
		.amdhsa_user_sgpr_kernarg_preload_length 0
		.amdhsa_user_sgpr_kernarg_preload_offset 0
		.amdhsa_user_sgpr_private_segment_size 0
		.amdhsa_uses_dynamic_stack 0
		.amdhsa_enable_private_segment 0
		.amdhsa_system_sgpr_workgroup_id_x 1
		.amdhsa_system_sgpr_workgroup_id_y 0
		.amdhsa_system_sgpr_workgroup_id_z 0
		.amdhsa_system_sgpr_workgroup_info 0
		.amdhsa_system_vgpr_workitem_id 0
		.amdhsa_next_free_vgpr 256
		.amdhsa_next_free_sgpr 94
		.amdhsa_accum_offset 256
		.amdhsa_reserve_vcc 1
		.amdhsa_float_round_mode_32 0
		.amdhsa_float_round_mode_16_64 0
		.amdhsa_float_denorm_mode_32 3
		.amdhsa_float_denorm_mode_16_64 3
		.amdhsa_dx10_clamp 1
		.amdhsa_ieee_mode 1
		.amdhsa_fp16_overflow 0
		.amdhsa_tg_split 0
		.amdhsa_exception_fp_ieee_invalid_op 0
		.amdhsa_exception_fp_denorm_src 0
		.amdhsa_exception_fp_ieee_div_zero 0
		.amdhsa_exception_fp_ieee_overflow 0
		.amdhsa_exception_fp_ieee_underflow 0
		.amdhsa_exception_fp_ieee_inexact 0
		.amdhsa_exception_int_div_zero 0
	.end_amdhsa_kernel

amdhsa.kernels:
  - .agpr_count:     0
    .args:
      - .actual_access:  read_only
        .address_space:  global
        .offset:         0
        .size:           8
        .value_kind:     global_buffer
      - .actual_access:  write_only
        .address_space:  global
        .offset:         8
        .size:           8
        .value_kind:     global_buffer
      - .offset:         16
        .size:           4
        .value_kind:     by_value
      - .actual_access:  read_only
        .address_space:  global
        .offset:         24
        .size:           8
        .value_kind:     global_buffer
      - .actual_access:  read_only
        .address_space:  global
        .offset:         32
        .size:           8
        .value_kind:     global_buffer
      - .actual_access:  read_only
        .address_space:  global
        .offset:         40
        .size:           8
        .value_kind:     global_buffer
      - .actual_access:  read_only
        .address_space:  global
        .offset:         48
        .size:           8
        .value_kind:     global_buffer
      - .actual_access:  write_only
        .address_space:  global
        .offset:         56
        .size:           8
        .value_kind:     global_buffer
      - .actual_access:  write_only
        .address_space:  global
        .offset:         64
        .size:           8
        .value_kind:     global_buffer
      - .actual_access:  write_only
        .address_space:  global
        .offset:         72
        .size:           8
        .value_kind:     global_buffer
    .group_segment_fixed_size: 16640
    .kernarg_segment_align: 8
    .kernarg_segment_size: 80
    .language:       OpenCL C
    .language_version:
      - 2
      - 0
    .max_flat_workgroup_size: 256
    .name:           _Z6k_prepPK15HIP_vector_typeIfLj4EEPS_IjLj4EEiPKfS6_S6_S6_PtS7_PS_IfLj2EE
    .private_segment_fixed_size: 0
    .sgpr_count:     22
    .sgpr_spill_count: 0
    .symbol:         _Z6k_prepPK15HIP_vector_typeIfLj4EEPS_IjLj4EEiPKfS6_S6_S6_PtS7_PS_IfLj2EE.kd
    .uniform_work_group_size: 1
    .uses_dynamic_stack: false
    .vgpr_count:     45
    .vgpr_spill_count: 0
    .wavefront_size: 64
  - .agpr_count:     0
    .args:
      - .actual_access:  read_only
        .address_space:  global
        .offset:         0
        .size:           8
        .value_kind:     global_buffer
      - .actual_access:  write_only
        .address_space:  global
        .offset:         8
        .size:           8
        .value_kind:     global_buffer
      - .actual_access:  read_only
        .address_space:  global
        .offset:         16
        .size:           8
        .value_kind:     global_buffer
    .group_segment_fixed_size: 36928
    .kernarg_segment_align: 8
    .kernarg_segment_size: 24
    .language:       OpenCL C
    .language_version:
      - 2
      - 0
    .max_flat_workgroup_size: 256
    .name:           _Z5k_fftPKtPtPKDv2_f
    .private_segment_fixed_size: 0
    .sgpr_count:     23
    .sgpr_spill_count: 0
    .symbol:         _Z5k_fftPKtPtPKDv2_f.kd
    .uniform_work_group_size: 1
    .uses_dynamic_stack: false
    .vgpr_count:     128
    .vgpr_spill_count: 0
    .wavefront_size: 64
  - .agpr_count:     0
    .args:
      - .address_space:  global
        .offset:         0
        .size:           8
        .value_kind:     global_buffer
      - .address_space:  global
        .offset:         8
        .size:           8
        .value_kind:     global_buffer
      - .actual_access:  write_only
        .address_space:  global
        .offset:         16
        .size:           8
        .value_kind:     global_buffer
      - .actual_access:  read_only
        .address_space:  global
        .offset:         24
        .size:           8
        .value_kind:     global_buffer
      - .actual_access:  read_only
        .address_space:  global
        .offset:         32
        .size:           8
        .value_kind:     global_buffer
      - .actual_access:  read_only
        .address_space:  global
        .offset:         40
        .size:           8
        .value_kind:     global_buffer
      - .offset:         48
        .size:           4
        .value_kind:     by_value
      - .offset:         52
        .size:           4
        .value_kind:     by_value
    .group_segment_fixed_size: 1024
    .kernarg_segment_align: 8
    .kernarg_segment_size: 56
    .language:       OpenCL C
    .language_version:
      - 2
      - 0
    .max_flat_workgroup_size: 512
    .name:           _Z6k_gemmILi2EEvPKtS1_PvPKfS4_S4_ii
    .private_segment_fixed_size: 0
    .sgpr_count:     100
    .sgpr_spill_count: 0
    .symbol:         _Z6k_gemmILi2EEvPKtS1_PvPKfS4_S4_ii.kd
    .uniform_work_group_size: 1
    .uses_dynamic_stack: false
    .vgpr_count:     256
    .vgpr_spill_count: 0
    .wavefront_size: 64
  - .agpr_count:     0
    .args:
      - .address_space:  global
        .offset:         0
        .size:           8
        .value_kind:     global_buffer
      - .address_space:  global
        .offset:         8
        .size:           8
        .value_kind:     global_buffer
      - .actual_access:  write_only
        .address_space:  global
        .offset:         16
        .size:           8
        .value_kind:     global_buffer
      - .actual_access:  read_only
        .address_space:  global
        .offset:         24
        .size:           8
        .value_kind:     global_buffer
      - .actual_access:  read_only
        .address_space:  global
        .offset:         32
        .size:           8
        .value_kind:     global_buffer
      - .actual_access:  read_only
        .address_space:  global
        .offset:         40
        .size:           8
        .value_kind:     global_buffer
      - .offset:         48
        .size:           4
        .value_kind:     by_value
      - .offset:         52
        .size:           4
        .value_kind:     by_value
    .group_segment_fixed_size: 1024
    .kernarg_segment_align: 8
    .kernarg_segment_size: 56
    .language:       OpenCL C
    .language_version:
      - 2
      - 0
    .max_flat_workgroup_size: 512
    .name:           _Z6k_gemmILi4EEvPKtS1_PvPKfS4_S4_ii
    .private_segment_fixed_size: 0
    .sgpr_count:     66
    .sgpr_spill_count: 0
    .symbol:         _Z6k_gemmILi4EEvPKtS1_PvPKfS4_S4_ii.kd
    .uniform_work_group_size: 1
    .uses_dynamic_stack: false
    .vgpr_count:     256
    .vgpr_spill_count: 0
    .wavefront_size: 64
